# routing-weight batching restricted to the first-rank epilogue path (second-rank path untouched)
# baseline (speedup 1.0000x reference)
.LBB0_1451:
	s_lshl_b32 s86, s85, 8
	s_add_i32 s86, s86, s94
	v_or_b32_e32 v192, s86, v49
	v_ashrrev_i32_e32 v193, 31, v192
	v_lshl_add_u64 v[130:131], v[192:193], 2, s[64:65]
	global_load_dword v194, v[130:131], off
	global_load_dword v190, v[130:131], off offset:64
	global_load_dword v188, v[130:131], off offset:128
	global_load_dword v186, v[130:131], off offset:192
	global_load_dword v176, v[130:131], off offset:512
	global_load_dword v174, v[130:131], off offset:576
	global_load_dword v172, v[130:131], off offset:640
	global_load_dword v168, v[130:131], off offset:704
	s_lshl_b32 s6, s83, 8
	s_or_b32 s83, s6, s95
	v_or_b32_e32 v138, 16, v192
	v_or_b32_e32 v140, 32, v192
	v_or_b32_e32 v142, 48, v192
	v_add_u32_e32 v178, 0x80, v192
	v_add_u32_e32 v180, 0x90, v192
	v_add_u32_e32 v182, 0xa0, v192
	v_add_u32_e32 v184, 0xb0, v192
	v_or_b32_e32 v170, s83, v201
	v_ashrrev_i32_e32 v139, 31, v138
	v_ashrrev_i32_e32 v141, 31, v140
	v_ashrrev_i32_e32 v143, 31, v142
	v_ashrrev_i32_e32 v179, 31, v178
	v_ashrrev_i32_e32 v181, 31, v180
	v_ashrrev_i32_e32 v183, 31, v182
	v_ashrrev_i32_e32 v185, 31, v184
	s_cmp_lt_i32 s85, s60
	v_ashrrev_i32_e32 v171, 31, v170
	s_waitcnt vmcnt(0)
	v_cmp_lt_i32_e32 vcc, -1, v194
	s_cbranch_scc1 .LBB0_1464
	v_lshl_add_u64 v[228:229], v[192:193], 2, s[66:67]
	global_load_dword v220, v[228:229], off
	global_load_dword v221, v[228:229], off offset:64
	global_load_dword v222, v[228:229], off offset:128
	global_load_dword v223, v[228:229], off offset:192
	global_load_dword v224, v[228:229], off offset:512
	global_load_dword v225, v[228:229], off offset:576
	global_load_dword v226, v[228:229], off offset:640
	global_load_dword v227, v[228:229], off offset:704
	s_waitcnt vmcnt(0)
	s_and_saveexec_b64 s[6:7], vcc
	s_cbranch_execz .LBB0_1486
	v_mov_b32_e32 v134, v220
	v_mov_b32_e32 v195, v48
	v_lshlrev_b64 v[130:131], 11, v[194:195]
	v_lshl_add_u64 v[130:131], s[58:59], 0, v[130:131]
	v_lshl_add_u64 v[136:137], v[170:171], 1, v[130:131]
	v_pk_mul_f32 v[132:133], v[124:125], v[134:135] op_sel_hi:[1,0]
	v_pk_mul_f32 v[130:131], v[122:123], v[134:135] op_sel_hi:[1,0]
	v_pk_mul_f32 v[144:145], v[128:129], v[134:135] op_sel_hi:[1,0]
	v_pk_mul_f32 v[146:147], v[126:127], v[134:135] op_sel_hi:[1,0]
	v_cvt_pk_bf16_f32 v130, v130, v131
	v_cvt_pk_bf16_f32 v131, v132, v133
	v_cvt_pk_bf16_f32 v132, v146, v147
	v_cvt_pk_bf16_f32 v133, v144, v145
	global_store_dwordx4 v[136:137], v[130:133], off
	v_pk_mul_f32 v[144:145], v[116:117], v[134:135] op_sel_hi:[1,0]
	s_nop 0
	v_pk_mul_f32 v[132:133], v[120:121], v[134:135] op_sel_hi:[1,0]
	v_pk_mul_f32 v[130:131], v[118:119], v[134:135] op_sel_hi:[1,0]
	v_pk_mul_f32 v[134:135], v[114:115], v[134:135] op_sel_hi:[1,0]
	v_cvt_pk_bf16_f32 v130, v130, v131
	v_cvt_pk_bf16_f32 v131, v132, v133
	v_cvt_pk_bf16_f32 v132, v134, v135
	v_cvt_pk_bf16_f32 v133, v144, v145
	global_store_dwordx4 v[136:137], v[130:133], off offset:256
	s_or_b64 exec, exec, s[6:7]
	v_cmp_lt_i32_e32 vcc, -1, v190
	s_and_saveexec_b64 s[6:7], vcc
	s_cbranch_execnz .LBB0_1487
